# v95 + back-edge rotation (lite) on the P1 / P8 / P10 K-loops: loop-carried scalar updates and exit compare moved in front of the loop-back barrier
# baseline (speedup 1.0000x reference)
; #define PG8_STAGE(bufoff, gbase, voff) do { _Pragma("unroll") for (int _i = 0; _i < 2; ++_i) \
;         __builtin_amdgcn_global_load_lds((const unsigned*)((const char*)(gbase) + _i * rstep64 + (voff)), (PG8_LAS unsigned*)(lds + (bufoff) + ldsw + _i * 8192), 16, 0, 0); } while (0)
; #define PG8_WAIT_V(n) asm volatile("s_waitcnt vmcnt(" #n ")" ::: "memory")
; #define PG8_WAIT_L(n) asm volatile("s_waitcnt lgkmcnt(" #n ")" ::: "memory")
; #define PG8_BAR __builtin_amdgcn_s_barrier()
; #define PG8_SCHED __builtin_amdgcn_sched_barrier(0)
;     ...
;             const char* a1 = cA + (size_t)(t + 1) * kstep;
;             const char* a2 = last ? nA : cA + (size_t)(t + 2) * kstep; const char* b2 = last ? nB : cB + (size_t)(t + 2) * kstep;
;             const char* a3 = a2 + kstep; const char* b3 = b2 + kstep;
;             if (last && has_next) S.a_ready(nxt);
;             if constexpr (SP2) {
;             PG8_LDB(B0, 0, 0); PG8_LDB(B1, 0, 1); PG8_SCHED; PG8_LDA(At, 0, 0); PG8_STAGE(PG8_SA(1, 1), a1 + hstep, voffA);
;             PG8_WAIT_V(8); PG8_WAIT_L(0); PG8_BAR; PG8_MMA(0, 0, At, B0); PG8_MMA(0, 1, At, B1); PG8_BAR; PG8_SCHED;
;             PG8_LDA(At, 0, 1); PG8_STAGE(PG8_SB(0, 0), b2, voffB); PG8_STAGE(PG8_SB(0, 1), b2 + hstep, voffB); PG8_STAGE(PG8_SA(0, 0), a2, voffA);
;             PG8_WAIT_V(8); PG8_WAIT_L(0); PG8_BAR; PG8_MMA(1, 0, At, B0); PG8_MMA(1, 1, At, B1); PG8_BAR; PG8_SCHED;
;             PG8_LDB(B0, 1, 0); PG8_LDB(B1, 1, 1); PG8_SCHED; PG8_LDA(At, 1, 0); PG8_STAGE(PG8_SA(0, 1), a2 + hstep, voffA);
;             PG8_WAIT_V(8); PG8_WAIT_L(0); PG8_BAR; PG8_MMA(0, 0, At, B0); PG8_MMA(0, 1, At, B1); PG8_BAR; PG8_SCHED;
;             PG8_LDA(At, 1, 1); PG8_STAGE(PG8_SB(1, 0), b3, voffB); PG8_STAGE(PG8_SB(1, 1), b3 + hstep, voffB); PG8_STAGE(PG8_SA(1, 0), a3, voffA);
;             PG8_WAIT_V(8); PG8_WAIT_L(0); PG8_BAR; PG8_MMA(1, 0, At, B0); PG8_MMA(1, 1, At, B1); PG8_BAR; PG8_SCHED;
.LBB0_113:
	ds_read_b128 v[142:145], v131
	ds_read_b128 v[150:153], v131 offset:1024
	ds_read_b128 v[154:157], v131 offset:2048
	ds_read_b128 v[158:161], v131 offset:3072
	ds_read_b128 v[162:165], v148
	ds_read_b128 v[166:169], v148 offset:1024
	ds_read_b128 v[170:173], v148 offset:2048
	ds_read_b128 v[174:177], v148 offset:3072
	s_add_u32 s82, s70, 0xfff80080
	s_addc_u32 s83, s71, -1
	s_cmp_eq_u32 s81, 28
	s_cselect_b32 s83, s5, s83
	s_cselect_b32 s82, s63, s82
	s_cselect_b32 s97, s61, s79
	s_cselect_b32 s96, s80, s78
	v_lshl_add_u64 v[146:147], s[70:71], 0, v[136:137]
	s_add_i32 m0, s75, 0xc000
	ds_read_b128 v[178:181], v149
	ds_read_b128 v[182:185], v149 offset:1024
	ds_read_b128 v[186:189], v149 offset:2048
	ds_read_b128 v[190:193], v149 offset:3072
	ds_read_b128 v[194:197], v149 offset:4096
	ds_read_b128 v[198:201], v149 offset:5120
	ds_read_b128 v[202:205], v149 offset:6144
	ds_read_b128 v[206:209], v149 offset:7168
	global_load_lds_dwordx4 v[146:147], off
	v_lshl_add_u64 v[146:147], v[146:147], 0, s[6:7]
	s_add_i32 m0, s75, 0xe000
	s_nop 0
	global_load_lds_dwordx4 v[146:147], off
	s_waitcnt vmcnt(8)
	s_waitcnt lgkmcnt(0)
	s_barrier
	s_setprio 1
	s_waitcnt lgkmcnt(0)
	v_mfma_i32_16x16x64_i8 v[126:129], v[142:145], v[178:181], v[126:129]
	v_mfma_i32_16x16x64_i8 v[122:125], v[154:157], v[178:181], v[122:125]
	v_mfma_i32_16x16x64_i8 v[110:113], v[142:145], v[186:189], v[110:113]
	v_mfma_i32_16x16x64_i8 v[106:109], v[154:157], v[186:189], v[106:109]
	v_mfma_i32_16x16x64_i8 v[94:97], v[142:145], v[194:197], v[94:97]
	v_mfma_i32_16x16x64_i8 v[90:93], v[154:157], v[194:197], v[90:93]
	v_mfma_i32_16x16x64_i8 v[78:81], v[142:145], v[202:205], v[78:81]
	v_mfma_i32_16x16x64_i8 v[74:77], v[154:157], v[202:205], v[74:77]
	v_mfma_i32_16x16x64_i8 v[126:129], v[150:153], v[182:185], v[126:129]
	v_mfma_i32_16x16x64_i8 v[122:125], v[158:161], v[182:185], v[122:125]
	v_mfma_i32_16x16x64_i8 v[110:113], v[150:153], v[190:193], v[110:113]
	v_mfma_i32_16x16x64_i8 v[106:109], v[158:161], v[190:193], v[106:109]
	v_mfma_i32_16x16x64_i8 v[94:97], v[150:153], v[198:201], v[94:97]
	v_mfma_i32_16x16x64_i8 v[90:93], v[158:161], v[198:201], v[90:93]
	v_mfma_i32_16x16x64_i8 v[78:81], v[150:153], v[206:209], v[78:81]
	v_mfma_i32_16x16x64_i8 v[74:77], v[158:161], v[206:209], v[74:77]
	s_setprio 0
	s_setprio 1
	v_mfma_i32_16x16x64_i8 v[118:121], v[162:165], v[178:181], v[118:121]
	v_mfma_i32_16x16x64_i8 v[114:117], v[170:173], v[178:181], v[114:117]
	v_mfma_i32_16x16x64_i8 v[102:105], v[162:165], v[186:189], v[102:105]
	v_mfma_i32_16x16x64_i8 v[98:101], v[170:173], v[186:189], v[98:101]
	v_mfma_i32_16x16x64_i8 v[86:89], v[162:165], v[194:197], v[86:89]
	v_mfma_i32_16x16x64_i8 v[82:85], v[170:173], v[194:197], v[82:85]
	v_mfma_i32_16x16x64_i8 v[70:73], v[162:165], v[202:205], v[70:73]
	v_mfma_i32_16x16x64_i8 v[66:69], v[170:173], v[202:205], v[66:69]
	v_mfma_i32_16x16x64_i8 v[118:121], v[166:169], v[182:185], v[118:121]
	v_mfma_i32_16x16x64_i8 v[114:117], v[174:177], v[182:185], v[114:117]
	v_mfma_i32_16x16x64_i8 v[102:105], v[166:169], v[190:193], v[102:105]
	v_mfma_i32_16x16x64_i8 v[98:101], v[174:177], v[190:193], v[98:101]
	v_mfma_i32_16x16x64_i8 v[86:89], v[166:169], v[198:201], v[86:89]
	v_mfma_i32_16x16x64_i8 v[82:85], v[174:177], v[198:201], v[82:85]
	v_mfma_i32_16x16x64_i8 v[70:73], v[166:169], v[206:209], v[70:73]
	v_mfma_i32_16x16x64_i8 v[66:69], v[174:177], v[206:209], v[66:69]
	s_setprio 0
	s_barrier
	v_lshl_add_u64 v[146:147], s[96:97], 0, v[134:135]
	s_add_i32 s96, s94, s77
	s_mov_b32 m0, s96
	ds_read_b128 v[178:181], v149 offset:16384
	ds_read_b128 v[182:185], v149 offset:17408
	ds_read_b128 v[186:189], v149 offset:18432
	ds_read_b128 v[190:193], v149 offset:19456
	ds_read_b128 v[194:197], v149 offset:20480
	ds_read_b128 v[198:201], v149 offset:21504
	ds_read_b128 v[202:205], v149 offset:22528
	ds_read_b128 v[206:209], v149 offset:23552
	global_load_lds_dwordx4 v[146:147], off
	v_lshl_add_u64 v[210:211], v[146:147], 0, s[6:7]
	s_add_i32 m0, s96, 0x2000
	s_add_i32 s96, s95, s77
	global_load_lds_dwordx4 v[210:211], off
	v_lshl_add_u64 v[210:211], v[146:147], 0, s[8:9]
	s_mov_b32 m0, s96
	s_nop 0
	global_load_lds_dwordx4 v[210:211], off
	v_lshl_add_u64 v[210:211], v[146:147], 0, s[10:11]
	s_add_i32 m0, s96, 0x2000
	s_nop 0
	global_load_lds_dwordx4 v[210:211], off
	v_lshl_add_u64 v[210:211], s[82:83], 0, v[132:133]
	s_mov_b32 m0, s75
	v_lshl_add_u64 v[212:213], v[210:211], 0, s[6:7]
	global_load_lds_dwordx4 v[210:211], off
	s_mov_b32 m0, s84
	s_nop 0
	global_load_lds_dwordx4 v[212:213], off
	s_waitcnt vmcnt(8)
	s_waitcnt lgkmcnt(0)
	s_barrier
; #define PG8_STAGE(bufoff, gbase, voff) do { _Pragma("unroll") for (int _i = 0; _i < 2; ++_i) \
;         __builtin_amdgcn_global_load_lds((const unsigned*)((const char*)(gbase) + _i * rstep64 + (voff)), (PG8_LAS unsigned*)(lds + (bufoff) + ldsw + _i * 8192), 16, 0, 0); } while (0)
; #define PG8_WAIT_V(n) asm volatile("s_waitcnt vmcnt(" #n ")" ::: "memory")
; #define PG8_WAIT_L(n) asm volatile("s_waitcnt lgkmcnt(" #n ")" ::: "memory")
; #define PG8_BAR __builtin_amdgcn_s_barrier()
; #define PG8_SCHED __builtin_amdgcn_sched_barrier(0)
;     ...
;             PG8_LDB(B0, 0, 0); PG8_LDB(B1, 0, 1); PG8_SCHED; PG8_LDA(At, 0, 0); PG8_STAGE(PG8_SA(1, 1), a1 + hstep, voffA);
;             PG8_WAIT_V(8); PG8_WAIT_L(0); PG8_BAR; PG8_MMA(0, 0, At, B0); PG8_MMA(0, 1, At, B1); PG8_BAR; PG8_SCHED;
;             PG8_LDA(At, 0, 1); PG8_STAGE(PG8_SB(0, 0), b2, voffB); PG8_STAGE(PG8_SB(0, 1), b2 + hstep, voffB); PG8_STAGE(PG8_SA(0, 0), a2, voffA);
;             PG8_WAIT_V(8); PG8_WAIT_L(0); PG8_BAR; PG8_MMA(1, 0, At, B0); PG8_MMA(1, 1, At, B1); PG8_BAR; PG8_SCHED;
;             PG8_LDB(B0, 1, 0); PG8_LDB(B1, 1, 1); PG8_SCHED; PG8_LDA(At, 1, 0); PG8_STAGE(PG8_SA(0, 1), a2 + hstep, voffA);
;             PG8_WAIT_V(8); PG8_WAIT_L(0); PG8_BAR; PG8_MMA(0, 0, At, B0); PG8_MMA(0, 1, At, B1); PG8_BAR; PG8_SCHED;
;             PG8_LDA(At, 1, 1); PG8_STAGE(PG8_SB(1, 0), b3, voffB); PG8_STAGE(PG8_SB(1, 1), b3 + hstep, voffB); PG8_STAGE(PG8_SA(1, 0), a3, voffA);
;             PG8_WAIT_V(8); PG8_WAIT_L(0); PG8_BAR; PG8_MMA(1, 0, At, B0); PG8_MMA(1, 1, At, B1); PG8_BAR; PG8_SCHED;
	s_setprio 1
	s_waitcnt lgkmcnt(0)
	v_mfma_i32_16x16x64_i8 v[62:65], v[142:145], v[178:181], v[62:65]
	v_mfma_i32_16x16x64_i8 v[58:61], v[154:157], v[178:181], v[58:61]
	v_mfma_i32_16x16x64_i8 v[46:49], v[142:145], v[186:189], v[46:49]
	v_mfma_i32_16x16x64_i8 v[42:45], v[154:157], v[186:189], v[42:45]
	v_mfma_i32_16x16x64_i8 v[30:33], v[142:145], v[194:197], v[30:33]
	v_mfma_i32_16x16x64_i8 v[26:29], v[154:157], v[194:197], v[26:29]
	v_mfma_i32_16x16x64_i8 v[14:17], v[142:145], v[202:205], v[14:17]
	v_mfma_i32_16x16x64_i8 v[10:13], v[154:157], v[202:205], v[10:13]
	v_mfma_i32_16x16x64_i8 v[62:65], v[150:153], v[182:185], v[62:65]
	v_mfma_i32_16x16x64_i8 v[58:61], v[158:161], v[182:185], v[58:61]
	v_mfma_i32_16x16x64_i8 v[46:49], v[150:153], v[190:193], v[46:49]
	v_mfma_i32_16x16x64_i8 v[42:45], v[158:161], v[190:193], v[42:45]
	v_mfma_i32_16x16x64_i8 v[30:33], v[150:153], v[198:201], v[30:33]
	v_mfma_i32_16x16x64_i8 v[26:29], v[158:161], v[198:201], v[26:29]
	v_mfma_i32_16x16x64_i8 v[14:17], v[150:153], v[206:209], v[14:17]
	v_mfma_i32_16x16x64_i8 v[10:13], v[158:161], v[206:209], v[10:13]
	s_setprio 0
	s_setprio 1
	v_mfma_i32_16x16x64_i8 v[54:57], v[162:165], v[178:181], v[54:57]
	v_mfma_i32_16x16x64_i8 v[50:53], v[170:173], v[178:181], v[50:53]
	v_mfma_i32_16x16x64_i8 v[38:41], v[162:165], v[186:189], v[38:41]
	v_mfma_i32_16x16x64_i8 v[34:37], v[170:173], v[186:189], v[34:37]
	v_mfma_i32_16x16x64_i8 v[22:25], v[162:165], v[194:197], v[22:25]
	v_mfma_i32_16x16x64_i8 v[18:21], v[170:173], v[194:197], v[18:21]
	v_mfma_i32_16x16x64_i8 v[6:9], v[162:165], v[202:205], v[6:9]
	v_mfma_i32_16x16x64_i8 v[2:5], v[170:173], v[202:205], v[2:5]
	v_mfma_i32_16x16x64_i8 v[54:57], v[166:169], v[182:185], v[54:57]
	v_mfma_i32_16x16x64_i8 v[50:53], v[174:177], v[182:185], v[50:53]
	v_mfma_i32_16x16x64_i8 v[38:41], v[166:169], v[190:193], v[38:41]
	v_mfma_i32_16x16x64_i8 v[34:37], v[174:177], v[190:193], v[34:37]
	v_mfma_i32_16x16x64_i8 v[22:25], v[166:169], v[198:201], v[22:25]
	v_mfma_i32_16x16x64_i8 v[18:21], v[174:177], v[198:201], v[18:21]
	v_mfma_i32_16x16x64_i8 v[6:9], v[166:169], v[206:209], v[6:9]
	v_mfma_i32_16x16x64_i8 v[2:5], v[174:177], v[206:209], v[2:5]
	s_setprio 0
	s_barrier
	s_add_i32 s82, 0, 0x18000
	s_add_i32 s83, 0, 0x1c000
	v_add_u32_e32 v158, s82, v1
	v_add_u32_e32 v174, s83, v1
	ds_read_b128 v[142:145], v158
	ds_read_b128 v[150:153], v158 offset:1024
	ds_read_b128 v[154:157], v158 offset:2048
	ds_read_b128 v[158:161], v158 offset:3072
	ds_read_b128 v[162:165], v174
	ds_read_b128 v[166:169], v174 offset:1024
	ds_read_b128 v[170:173], v174 offset:2048
	ds_read_b128 v[174:177], v174 offset:3072
	s_mov_b32 m0, s85
	v_lshl_add_u64 v[212:213], v[210:211], 0, s[8:9]
	ds_read_b128 v[178:181], v149 offset:32768
	ds_read_b128 v[182:185], v149 offset:33792
	ds_read_b128 v[186:189], v149 offset:34816
	ds_read_b128 v[190:193], v149 offset:35840
	ds_read_b128 v[194:197], v149 offset:36864
	ds_read_b128 v[198:201], v149 offset:37888
	ds_read_b128 v[202:205], v149 offset:38912
	ds_read_b128 v[206:209], v149 offset:39936
	global_load_lds_dwordx4 v[212:213], off
	v_lshl_add_u64 v[212:213], v[210:211], 0, s[10:11]
	s_mov_b32 m0, s86
	s_nop 0
	global_load_lds_dwordx4 v[212:213], off
	s_waitcnt vmcnt(8)
	s_waitcnt lgkmcnt(0)
	s_barrier
	s_setprio 1
	s_waitcnt lgkmcnt(0)
	v_mfma_i32_16x16x64_i8 v[126:129], v[142:145], v[178:181], v[126:129]
	v_mfma_i32_16x16x64_i8 v[122:125], v[154:157], v[178:181], v[122:125]
	v_mfma_i32_16x16x64_i8 v[110:113], v[142:145], v[186:189], v[110:113]
	v_mfma_i32_16x16x64_i8 v[106:109], v[154:157], v[186:189], v[106:109]
	v_mfma_i32_16x16x64_i8 v[94:97], v[142:145], v[194:197], v[94:97]
	v_mfma_i32_16x16x64_i8 v[90:93], v[154:157], v[194:197], v[90:93]
	v_mfma_i32_16x16x64_i8 v[78:81], v[142:145], v[202:205], v[78:81]
	v_mfma_i32_16x16x64_i8 v[74:77], v[154:157], v[202:205], v[74:77]
	v_mfma_i32_16x16x64_i8 v[126:129], v[150:153], v[182:185], v[126:129]
	v_mfma_i32_16x16x64_i8 v[122:125], v[158:161], v[182:185], v[122:125]
	v_mfma_i32_16x16x64_i8 v[110:113], v[150:153], v[190:193], v[110:113]
	v_mfma_i32_16x16x64_i8 v[106:109], v[158:161], v[190:193], v[106:109]
	v_mfma_i32_16x16x64_i8 v[94:97], v[150:153], v[198:201], v[94:97]
	v_mfma_i32_16x16x64_i8 v[90:93], v[158:161], v[198:201], v[90:93]
	v_mfma_i32_16x16x64_i8 v[78:81], v[150:153], v[206:209], v[78:81]
	v_mfma_i32_16x16x64_i8 v[74:77], v[158:161], v[206:209], v[74:77]
	s_setprio 0
	s_setprio 1
	v_mfma_i32_16x16x64_i8 v[118:121], v[162:165], v[178:181], v[118:121]
	v_mfma_i32_16x16x64_i8 v[114:117], v[170:173], v[178:181], v[114:117]
	v_mfma_i32_16x16x64_i8 v[102:105], v[162:165], v[186:189], v[102:105]
	v_mfma_i32_16x16x64_i8 v[98:101], v[170:173], v[186:189], v[98:101]
	v_mfma_i32_16x16x64_i8 v[86:89], v[162:165], v[194:197], v[86:89]
	v_mfma_i32_16x16x64_i8 v[82:85], v[170:173], v[194:197], v[82:85]
	v_mfma_i32_16x16x64_i8 v[70:73], v[162:165], v[202:205], v[70:73]
	v_mfma_i32_16x16x64_i8 v[66:69], v[170:173], v[202:205], v[66:69]
	v_mfma_i32_16x16x64_i8 v[118:121], v[166:169], v[182:185], v[118:121]
	v_mfma_i32_16x16x64_i8 v[114:117], v[174:177], v[182:185], v[114:117]
	v_mfma_i32_16x16x64_i8 v[102:105], v[166:169], v[190:193], v[102:105]
	v_mfma_i32_16x16x64_i8 v[98:101], v[174:177], v[190:193], v[98:101]
	v_mfma_i32_16x16x64_i8 v[86:89], v[166:169], v[198:201], v[86:89]
	v_mfma_i32_16x16x64_i8 v[82:85], v[174:177], v[198:201], v[82:85]
	v_mfma_i32_16x16x64_i8 v[70:73], v[166:169], v[206:209], v[70:73]
	v_mfma_i32_16x16x64_i8 v[66:69], v[174:177], v[206:209], v[66:69]
	s_setprio 0
	s_barrier
; #define PG8_STAGE(bufoff, gbase, voff) do { _Pragma("unroll") for (int _i = 0; _i < 2; ++_i) \
;         __builtin_amdgcn_global_load_lds((const unsigned*)((const char*)(gbase) + _i * rstep64 + (voff)), (PG8_LAS unsigned*)(lds + (bufoff) + ldsw + _i * 8192), 16, 0, 0); } while (0)
; #define PG8_WAIT_V(n) asm volatile("s_waitcnt vmcnt(" #n ")" ::: "memory")
; #define PG8_WAIT_L(n) asm volatile("s_waitcnt lgkmcnt(" #n ")" ::: "memory")
; #define PG8_BAR __builtin_amdgcn_s_barrier()
; #define PG8_SCHED __builtin_amdgcn_sched_barrier(0)
;     ...
;             PG8_WAIT_V(8); PG8_WAIT_L(0); PG8_BAR; PG8_MMA(1, 0, At, B0); PG8_MMA(1, 1, At, B1); PG8_BAR; PG8_SCHED;
;             PG8_LDB(B0, 1, 0); PG8_LDB(B1, 1, 1); PG8_SCHED; PG8_LDA(At, 1, 0); PG8_STAGE(PG8_SA(0, 1), a2 + hstep, voffA);
;             PG8_WAIT_V(8); PG8_WAIT_L(0); PG8_BAR; PG8_MMA(0, 0, At, B0); PG8_MMA(0, 1, At, B1); PG8_BAR; PG8_SCHED;
;             PG8_LDA(At, 1, 1); PG8_STAGE(PG8_SB(1, 0), b3, voffB); PG8_STAGE(PG8_SB(1, 1), b3 + hstep, voffB); PG8_STAGE(PG8_SA(1, 0), a3, voffA);
;             PG8_WAIT_V(8); PG8_WAIT_L(0); PG8_BAR; PG8_MMA(1, 0, At, B0); PG8_MMA(1, 1, At, B1); PG8_BAR; PG8_SCHED;
	s_add_i32 s82, s82, s77
	v_lshl_add_u64 v[212:213], v[146:147], 0, s[46:47]
	s_mov_b32 m0, s82
	ds_read_b128 v[178:181], v149 offset:49152
	ds_read_b128 v[182:185], v149 offset:50176
	ds_read_b128 v[186:189], v149 offset:51200
	ds_read_b128 v[190:193], v149 offset:52224
	ds_read_b128 v[194:197], v149 offset:53248
	ds_read_b128 v[198:201], v149 offset:54272
	ds_read_b128 v[202:205], v149 offset:55296
	ds_read_b128 v[206:209], v149 offset:56320
	global_load_lds_dwordx4 v[212:213], off
	v_lshl_add_u64 v[212:213], v[146:147], 0, s[50:51]
	s_add_i32 m0, s82, 0x2000
	s_add_i32 s82, s83, s77
	global_load_lds_dwordx4 v[212:213], off
	v_lshl_add_u64 v[212:213], v[146:147], 0, s[52:53]
	s_mov_b32 m0, s82
	v_lshl_add_u64 v[146:147], v[146:147], 0, s[54:55]
	global_load_lds_dwordx4 v[212:213], off
	s_add_i32 m0, s82, 0x2000
	s_nop 0
	global_load_lds_dwordx4 v[146:147], off
	v_lshl_add_u64 v[146:147], v[210:211], 0, s[46:47]
	s_mov_b32 m0, s88
	s_nop 0
	global_load_lds_dwordx4 v[146:147], off
	v_lshl_add_u64 v[146:147], v[210:211], 0, s[50:51]
	s_mov_b32 m0, s89
	s_nop 0
	global_load_lds_dwordx4 v[146:147], off
	s_waitcnt vmcnt(8)
	s_waitcnt lgkmcnt(0)
	s_barrier
	s_setprio 1
	s_waitcnt lgkmcnt(0)
	v_mfma_i32_16x16x64_i8 v[62:65], v[142:145], v[178:181], v[62:65]
	v_mfma_i32_16x16x64_i8 v[58:61], v[154:157], v[178:181], v[58:61]
	v_mfma_i32_16x16x64_i8 v[46:49], v[142:145], v[186:189], v[46:49]
	v_mfma_i32_16x16x64_i8 v[42:45], v[154:157], v[186:189], v[42:45]
	v_mfma_i32_16x16x64_i8 v[30:33], v[142:145], v[194:197], v[30:33]
	v_mfma_i32_16x16x64_i8 v[26:29], v[154:157], v[194:197], v[26:29]
	v_mfma_i32_16x16x64_i8 v[14:17], v[142:145], v[202:205], v[14:17]
	v_mfma_i32_16x16x64_i8 v[10:13], v[154:157], v[202:205], v[10:13]
	v_mfma_i32_16x16x64_i8 v[62:65], v[150:153], v[182:185], v[62:65]
	v_mfma_i32_16x16x64_i8 v[58:61], v[158:161], v[182:185], v[58:61]
	v_mfma_i32_16x16x64_i8 v[46:49], v[150:153], v[190:193], v[46:49]
	v_mfma_i32_16x16x64_i8 v[42:45], v[158:161], v[190:193], v[42:45]
	v_mfma_i32_16x16x64_i8 v[30:33], v[150:153], v[198:201], v[30:33]
	v_mfma_i32_16x16x64_i8 v[26:29], v[158:161], v[198:201], v[26:29]
	v_mfma_i32_16x16x64_i8 v[14:17], v[150:153], v[206:209], v[14:17]
	v_mfma_i32_16x16x64_i8 v[10:13], v[158:161], v[206:209], v[10:13]
	s_setprio 0
	s_setprio 1
	v_mfma_i32_16x16x64_i8 v[54:57], v[162:165], v[178:181], v[54:57]
	v_mfma_i32_16x16x64_i8 v[50:53], v[170:173], v[178:181], v[50:53]
	v_mfma_i32_16x16x64_i8 v[38:41], v[162:165], v[186:189], v[38:41]
	v_mfma_i32_16x16x64_i8 v[34:37], v[170:173], v[186:189], v[34:37]
	v_mfma_i32_16x16x64_i8 v[22:25], v[162:165], v[194:197], v[22:25]
	v_mfma_i32_16x16x64_i8 v[18:21], v[170:173], v[194:197], v[18:21]
	v_mfma_i32_16x16x64_i8 v[6:9], v[162:165], v[202:205], v[6:9]
	v_mfma_i32_16x16x64_i8 v[2:5], v[170:173], v[202:205], v[2:5]
	v_mfma_i32_16x16x64_i8 v[54:57], v[166:169], v[182:185], v[54:57]
	v_mfma_i32_16x16x64_i8 v[50:53], v[174:177], v[182:185], v[50:53]
	v_mfma_i32_16x16x64_i8 v[38:41], v[166:169], v[190:193], v[38:41]
	v_mfma_i32_16x16x64_i8 v[34:37], v[174:177], v[190:193], v[34:37]
	v_mfma_i32_16x16x64_i8 v[22:25], v[166:169], v[198:201], v[22:25]
	v_mfma_i32_16x16x64_i8 v[18:21], v[174:177], v[198:201], v[18:21]
	v_mfma_i32_16x16x64_i8 v[6:9], v[166:169], v[206:209], v[6:9]
	v_mfma_i32_16x16x64_i8 v[2:5], v[174:177], v[206:209], v[2:5]
	s_setprio 0
	s_add_i32 s81, s81, 2
	s_add_u32 s70, s70, 0x100
	s_addc_u32 s71, s71, 0
	s_add_u32 s78, s78, 0x100
	s_addc_u32 s79, s79, 0
	s_cmp_gt_u32 s81, 29
	s_barrier
	s_cbranch_scc0 .LBB0_113
	s_and_b64 vcc, exec, s[56:57]
	s_cbranch_vccz .LBB0_116
	s_barrier

; #define PG8_STAGE(bufoff, gbase, voff) do { _Pragma("unroll") for (int _i = 0; _i < 2; ++_i) \
;         __builtin_amdgcn_global_load_lds((const unsigned*)((const char*)(gbase) + _i * rstep64 + (voff)), (PG8_LAS unsigned*)(lds + (bufoff) + ldsw + _i * 8192), 16, 0, 0); } while (0)
; #define PG8_WAIT_V(n) asm volatile("s_waitcnt vmcnt(" #n ")" ::: "memory")
; #define PG8_WAIT_L(n) asm volatile("s_waitcnt lgkmcnt(" #n ")" ::: "memory")
; #define PG8_BAR __builtin_amdgcn_s_barrier()
; #define PG8_SCHED __builtin_amdgcn_sched_barrier(0)
;     ...
;             PG8_LDB(B0, 0, 0); PG8_LDB(B1, 0, 1); PG8_SCHED; PG8_LDA(At, 0, 0); PG8_STAGE(PG8_SA(1, 1), a1 + hstep, voffA);
;             PG8_WAIT_V(8); PG8_WAIT_L(0); PG8_BAR; PG8_MMA(0, 0, At, B0); PG8_MMA(0, 1, At, B1); PG8_BAR; PG8_SCHED;
;             PG8_LDA(At, 0, 1); PG8_STAGE(PG8_SB(0, 0), b2, voffB); PG8_STAGE(PG8_SB(0, 1), b2 + hstep, voffB); PG8_STAGE(PG8_SA(0, 0), a2, voffA);
;             PG8_WAIT_V(8); PG8_WAIT_L(0); PG8_BAR; PG8_MMA(1, 0, At, B0); PG8_MMA(1, 1, At, B1); PG8_BAR; PG8_SCHED;
;             PG8_LDB(B0, 1, 0); PG8_LDB(B1, 1, 1); PG8_SCHED; PG8_LDA(At, 1, 0); PG8_STAGE(PG8_SA(0, 1), a2 + hstep, voffA);
;             PG8_WAIT_V(8); PG8_WAIT_L(0); PG8_BAR; PG8_MMA(0, 0, At, B0); PG8_MMA(0, 1, At, B1); PG8_BAR; PG8_SCHED;
;             PG8_LDA(At, 1, 1); PG8_STAGE(PG8_SB(1, 0), b3, voffB); PG8_STAGE(PG8_SB(1, 1), b3 + hstep, voffB); PG8_STAGE(PG8_SA(1, 0), a3, voffA);
;             PG8_WAIT_V(8); PG8_WAIT_L(0); PG8_BAR; PG8_MMA(1, 0, At, B0); PG8_MMA(1, 1, At, B1); PG8_BAR; PG8_SCHED;
.LBB0_3064:
	ds_read_b128 v[146:149], v142
	ds_read_b128 v[150:153], v142 offset:1024
	ds_read_b128 v[154:157], v142 offset:2048
	ds_read_b128 v[158:161], v142 offset:3072
	ds_read_b128 v[162:165], v143
	ds_read_b128 v[166:169], v143 offset:1024
	ds_read_b128 v[170:173], v143 offset:2048
	ds_read_b128 v[174:177], v143 offset:3072
	s_add_u32 s52, s50, 0xfff80080
	s_addc_u32 s53, s51, -1
	s_cmp_eq_u32 s80, 28
	s_cselect_b32 s53, s43, s53
	s_cselect_b32 s52, s49, s52
	s_cselect_b32 s55, s41, s79
	s_cselect_b32 s54, s77, s78
	v_lshl_add_u64 v[138:139], s[50:51], 0, v[132:133]
	s_add_i32 m0, s58, 0xc000
	ds_read_b128 v[178:181], v144
	ds_read_b128 v[182:185], v144 offset:1024
	ds_read_b128 v[186:189], v144 offset:2048
	ds_read_b128 v[190:193], v144 offset:3072
	ds_read_b128 v[194:197], v144 offset:4096
	ds_read_b128 v[198:201], v144 offset:5120
	ds_read_b128 v[202:205], v144 offset:6144
	ds_read_b128 v[206:209], v144 offset:7168
	global_load_lds_dwordx4 v[138:139], off
	v_lshl_add_u64 v[138:139], v[138:139], 0, s[4:5]
	s_add_i32 m0, s58, 0xe000
	s_nop 0
	global_load_lds_dwordx4 v[138:139], off
	s_waitcnt vmcnt(8)
	s_waitcnt lgkmcnt(0)
	s_barrier
	s_setprio 1
	s_waitcnt lgkmcnt(0)
	v_mfma_scale_f32_16x16x128_f8f6f4 v[126:129], v[146:153], v[178:185], v[126:129], v145, v145 op_sel:[0,1,0] op_sel_hi:[0,0,0]
	v_mfma_scale_f32_16x16x128_f8f6f4 v[122:125], v[154:161], v[178:185], v[122:125], v145, v145 op_sel:[0,1,0] op_sel_hi:[0,0,0]
	v_mfma_scale_f32_16x16x128_f8f6f4 v[110:113], v[146:153], v[186:193], v[110:113], v145, v145 op_sel:[0,1,0] op_sel_hi:[0,0,0]
	v_mfma_scale_f32_16x16x128_f8f6f4 v[106:109], v[154:161], v[186:193], v[106:109], v145, v145 op_sel:[0,1,0] op_sel_hi:[0,0,0]
	v_mfma_scale_f32_16x16x128_f8f6f4 v[138:141], v[146:153], v[194:201], v[94:97], v145, v145 op_sel:[0,1,0] op_sel_hi:[0,0,0]
	v_mfma_scale_f32_16x16x128_f8f6f4 v[210:213], v[154:161], v[194:201], v[90:93], v145, v145 op_sel:[0,1,0] op_sel_hi:[0,0,0]
	v_mfma_scale_f32_16x16x128_f8f6f4 v[214:217], v[146:153], v[202:209], v[78:81], v145, v145 op_sel:[0,1,0] op_sel_hi:[0,0,0]
	v_mfma_scale_f32_16x16x128_f8f6f4 v[218:221], v[154:161], v[202:209], v[74:77], v145, v145 op_sel:[0,1,0] op_sel_hi:[0,0,0]
	s_setprio 0
	s_setprio 1
	v_mfma_scale_f32_16x16x128_f8f6f4 v[118:121], v[162:169], v[178:185], v[118:121], v145, v145 op_sel:[0,1,0] op_sel_hi:[0,0,0]
	v_mfma_scale_f32_16x16x128_f8f6f4 v[114:117], v[170:177], v[178:185], v[114:117], v145, v145 op_sel:[0,1,0] op_sel_hi:[0,0,0]
	v_mfma_scale_f32_16x16x128_f8f6f4 v[102:105], v[162:169], v[186:193], v[102:105], v145, v145 op_sel:[0,1,0] op_sel_hi:[0,0,0]
	v_mfma_scale_f32_16x16x128_f8f6f4 v[98:101], v[170:177], v[186:193], v[98:101], v145, v145 op_sel:[0,1,0] op_sel_hi:[0,0,0]
	v_mfma_scale_f32_16x16x128_f8f6f4 v[178:181], v[162:169], v[194:201], v[86:89], v145, v145 op_sel:[0,1,0] op_sel_hi:[0,0,0]
	v_mfma_scale_f32_16x16x128_f8f6f4 v[182:185], v[170:177], v[194:201], v[82:85], v145, v145 op_sel:[0,1,0] op_sel_hi:[0,0,0]
	v_mfma_scale_f32_16x16x128_f8f6f4 v[186:189], v[162:169], v[202:209], v[70:73], v145, v145 op_sel:[0,1,0] op_sel_hi:[0,0,0]
	v_mfma_scale_f32_16x16x128_f8f6f4 v[190:193], v[170:177], v[202:209], v[66:69], v145, v145 op_sel:[0,1,0] op_sel_hi:[0,0,0]
	s_setprio 0
	s_barrier
	v_lshl_add_u64 v[134:135], s[54:55], 0, v[130:131]
	s_add_i32 s54, s71, s57
	s_mov_b32 m0, s54
	s_nop 1
	ds_read_b128 v[66:69], v144 offset:16384
	ds_read_b128 v[70:73], v144 offset:17408
	ds_read_b128 v[74:77], v144 offset:18432
	ds_read_b128 v[78:81], v144 offset:19456
	ds_read_b128 v[82:85], v144 offset:20480
	ds_read_b128 v[86:89], v144 offset:21504
	ds_read_b128 v[90:93], v144 offset:22528
	ds_read_b128 v[94:97], v144 offset:23552
	global_load_lds_dwordx4 v[134:135], off
	v_lshl_add_u64 v[194:195], v[134:135], 0, s[4:5]
	s_add_i32 m0, s54, 0x2000
	s_add_i32 s54, s74, s57
	global_load_lds_dwordx4 v[194:195], off
	v_lshl_add_u64 v[194:195], v[134:135], 0, s[6:7]
	s_mov_b32 m0, s54
	v_lshl_add_u64 v[136:137], s[52:53], 0, v[130:131]
	global_load_lds_dwordx4 v[194:195], off
	v_lshl_add_u64 v[194:195], v[134:135], 0, s[8:9]
	s_add_i32 m0, s54, 0x2000
	s_nop 0
	global_load_lds_dwordx4 v[194:195], off
	s_mov_b32 m0, s58
	v_lshl_add_u64 v[194:195], v[136:137], 0, s[4:5]
	global_load_lds_dwordx4 v[136:137], off
	s_mov_b32 m0, s59
	s_nop 0
	global_load_lds_dwordx4 v[194:195], off
	s_waitcnt vmcnt(8)
	s_waitcnt lgkmcnt(0)
	s_barrier
	s_setprio 1
	s_waitcnt lgkmcnt(0)
	v_mfma_scale_f32_16x16x128_f8f6f4 v[62:65], v[146:153], v[66:73], v[62:65], v145, v145 op_sel:[0,1,0] op_sel_hi:[0,0,0]
	v_mfma_scale_f32_16x16x128_f8f6f4 v[58:61], v[154:161], v[66:73], v[58:61], v145, v145 op_sel:[0,1,0] op_sel_hi:[0,0,0]
	v_mfma_scale_f32_16x16x128_f8f6f4 v[194:197], v[146:153], v[74:81], v[46:49], v145, v145 op_sel:[0,1,0] op_sel_hi:[0,0,0]
	v_mfma_scale_f32_16x16x128_f8f6f4 v[198:201], v[154:161], v[74:81], v[42:45], v145, v145 op_sel:[0,1,0] op_sel_hi:[0,0,0]
	v_mfma_scale_f32_16x16x128_f8f6f4 v[202:205], v[146:153], v[82:89], v[30:33], v145, v145 op_sel:[0,1,0] op_sel_hi:[0,0,0]
	v_mfma_scale_f32_16x16x128_f8f6f4 v[206:209], v[154:161], v[82:89], v[26:29], v145, v145 op_sel:[0,1,0] op_sel_hi:[0,0,0]
	v_mfma_scale_f32_16x16x128_f8f6f4 v[222:225], v[146:153], v[90:97], v[14:17], v145, v145 op_sel:[0,1,0] op_sel_hi:[0,0,0]
	v_mfma_scale_f32_16x16x128_f8f6f4 v[226:229], v[154:161], v[90:97], v[10:13], v145, v145 op_sel:[0,1,0] op_sel_hi:[0,0,0]
	s_setprio 0
	s_setprio 1
	v_mfma_scale_f32_16x16x128_f8f6f4 v[54:57], v[162:169], v[66:73], v[54:57], v145, v145 op_sel:[0,1,0] op_sel_hi:[0,0,0]
	v_mfma_scale_f32_16x16x128_f8f6f4 v[50:53], v[170:177], v[66:73], v[50:53], v145, v145 op_sel:[0,1,0] op_sel_hi:[0,0,0]
	v_mfma_scale_f32_16x16x128_f8f6f4 v[230:233], v[162:169], v[74:81], v[38:41], v145, v145 op_sel:[0,1,0] op_sel_hi:[0,0,0]
	v_mfma_scale_f32_16x16x128_f8f6f4 v[234:237], v[170:177], v[74:81], v[34:37], v145, v145 op_sel:[0,1,0] op_sel_hi:[0,0,0]
	v_mfma_scale_f32_16x16x128_f8f6f4 v[238:241], v[162:169], v[82:89], v[22:25], v145, v145 op_sel:[0,1,0] op_sel_hi:[0,0,0]
	v_mfma_scale_f32_16x16x128_f8f6f4 v[242:245], v[170:177], v[82:89], v[18:21], v145, v145 op_sel:[0,1,0] op_sel_hi:[0,0,0]
	v_mfma_scale_f32_16x16x128_f8f6f4 v[246:249], v[162:169], v[90:97], v[6:9], v145, v145 op_sel:[0,1,0] op_sel_hi:[0,0,0]
	v_mfma_scale_f32_16x16x128_f8f6f4 v[250:253], v[170:177], v[90:97], v[2:5], v145, v145 op_sel:[0,1,0] op_sel_hi:[0,0,0]
	s_setprio 0
	s_barrier
; #define PG8_STAGE(bufoff, gbase, voff) do { _Pragma("unroll") for (int _i = 0; _i < 2; ++_i) \
;         __builtin_amdgcn_global_load_lds((const unsigned*)((const char*)(gbase) + _i * rstep64 + (voff)), (PG8_LAS unsigned*)(lds + (bufoff) + ldsw + _i * 8192), 16, 0, 0); } while (0)
; #define PG8_WAIT_V(n) asm volatile("s_waitcnt vmcnt(" #n ")" ::: "memory")
; #define PG8_WAIT_L(n) asm volatile("s_waitcnt lgkmcnt(" #n ")" ::: "memory")
; #define PG8_BAR __builtin_amdgcn_s_barrier()
; #define PG8_SCHED __builtin_amdgcn_sched_barrier(0)
;     ...
;             PG8_WAIT_V(8); PG8_WAIT_L(0); PG8_BAR; PG8_MMA(1, 0, At, B0); PG8_MMA(1, 1, At, B1); PG8_BAR; PG8_SCHED;
;             PG8_LDB(B0, 1, 0); PG8_LDB(B1, 1, 1); PG8_SCHED; PG8_LDA(At, 1, 0); PG8_STAGE(PG8_SA(0, 1), a2 + hstep, voffA);
;             PG8_WAIT_V(8); PG8_WAIT_L(0); PG8_BAR; PG8_MMA(0, 0, At, B0); PG8_MMA(0, 1, At, B1); PG8_BAR; PG8_SCHED;
;             PG8_LDA(At, 1, 1); PG8_STAGE(PG8_SB(1, 0), b3, voffB); PG8_STAGE(PG8_SB(1, 1), b3 + hstep, voffB); PG8_STAGE(PG8_SA(1, 0), a3, voffA);
;             PG8_WAIT_V(8); PG8_WAIT_L(0); PG8_BAR; PG8_MMA(1, 0, At, B0); PG8_MMA(1, 1, At, B1); PG8_BAR; PG8_SCHED;
	s_add_i32 s52, 0, 0x18000
	v_add_u32_e32 v10, s52, v1
	s_add_i32 s53, 0, 0x1c000
	s_nop 1
	ds_read_b128 v[2:5], v10
	ds_read_b128 v[6:9], v10 offset:1024
	ds_read_b128 v[18:21], v10 offset:2048
	ds_read_b128 v[22:25], v10 offset:3072
	v_add_u32_e32 v10, s53, v1
	ds_read_b128 v[146:149], v10
	ds_read_b128 v[150:153], v10 offset:1024
	ds_read_b128 v[154:157], v10 offset:2048
	ds_read_b128 v[158:161], v10 offset:3072
	s_mov_b32 m0, s60
	v_lshl_add_u64 v[66:67], v[136:137], 0, s[6:7]
	ds_read_b128 v[10:13], v144 offset:32768
	ds_read_b128 v[14:17], v144 offset:33792
	ds_read_b128 v[26:29], v144 offset:34816
	ds_read_b128 v[30:33], v144 offset:35840
	ds_read_b128 v[34:37], v144 offset:36864
	ds_read_b128 v[38:41], v144 offset:37888
	ds_read_b128 v[42:45], v144 offset:38912
	ds_read_b128 v[46:49], v144 offset:39936
	global_load_lds_dwordx4 v[66:67], off
	v_lshl_add_u64 v[66:67], v[136:137], 0, s[8:9]
	s_mov_b32 m0, s61
	s_nop 0
	global_load_lds_dwordx4 v[66:67], off
	s_waitcnt vmcnt(8)
	s_waitcnt lgkmcnt(0)
	s_barrier
	s_setprio 1
	s_waitcnt lgkmcnt(0)
	v_mfma_scale_f32_16x16x128_f8f6f4 v[126:129], v[2:9], v[10:17], v[126:129], v145, v145 op_sel:[0,1,0] op_sel_hi:[0,0,0]
	v_mfma_scale_f32_16x16x128_f8f6f4 v[122:125], v[18:25], v[10:17], v[122:125], v145, v145 op_sel:[0,1,0] op_sel_hi:[0,0,0]
	v_mfma_scale_f32_16x16x128_f8f6f4 v[110:113], v[2:9], v[26:33], v[110:113], v145, v145 op_sel:[0,1,0] op_sel_hi:[0,0,0]
	v_mfma_scale_f32_16x16x128_f8f6f4 v[106:109], v[18:25], v[26:33], v[106:109], v145, v145 op_sel:[0,1,0] op_sel_hi:[0,0,0]
	v_mfma_scale_f32_16x16x128_f8f6f4 v[94:97], v[2:9], v[34:41], v[138:141], v145, v145 op_sel:[0,1,0] op_sel_hi:[0,0,0]
	v_mfma_scale_f32_16x16x128_f8f6f4 v[90:93], v[18:25], v[34:41], v[210:213], v145, v145 op_sel:[0,1,0] op_sel_hi:[0,0,0]
	v_mfma_scale_f32_16x16x128_f8f6f4 v[78:81], v[2:9], v[42:49], v[214:217], v145, v145 op_sel:[0,1,0] op_sel_hi:[0,0,0]
	v_mfma_scale_f32_16x16x128_f8f6f4 v[74:77], v[18:25], v[42:49], v[218:221], v145, v145 op_sel:[0,1,0] op_sel_hi:[0,0,0]
	s_setprio 0
	s_setprio 1
	v_mfma_scale_f32_16x16x128_f8f6f4 v[118:121], v[146:153], v[10:17], v[118:121], v145, v145 op_sel:[0,1,0] op_sel_hi:[0,0,0]
	v_mfma_scale_f32_16x16x128_f8f6f4 v[114:117], v[154:161], v[10:17], v[114:117], v145, v145 op_sel:[0,1,0] op_sel_hi:[0,0,0]
	v_mfma_scale_f32_16x16x128_f8f6f4 v[102:105], v[146:153], v[26:33], v[102:105], v145, v145 op_sel:[0,1,0] op_sel_hi:[0,0,0]
	v_mfma_scale_f32_16x16x128_f8f6f4 v[98:101], v[154:161], v[26:33], v[98:101], v145, v145 op_sel:[0,1,0] op_sel_hi:[0,0,0]
	v_mfma_scale_f32_16x16x128_f8f6f4 v[86:89], v[146:153], v[34:41], v[178:181], v145, v145 op_sel:[0,1,0] op_sel_hi:[0,0,0]
	v_mfma_scale_f32_16x16x128_f8f6f4 v[82:85], v[154:161], v[34:41], v[182:185], v145, v145 op_sel:[0,1,0] op_sel_hi:[0,0,0]
	v_mfma_scale_f32_16x16x128_f8f6f4 v[70:73], v[146:153], v[42:49], v[186:189], v145, v145 op_sel:[0,1,0] op_sel_hi:[0,0,0]
	v_mfma_scale_f32_16x16x128_f8f6f4 v[66:69], v[154:161], v[42:49], v[190:193], v145, v145 op_sel:[0,1,0] op_sel_hi:[0,0,0]
	s_setprio 0
	s_barrier
	s_add_i32 s52, s52, s57
	v_lshl_add_u64 v[10:11], v[134:135], 0, s[18:19]
	s_mov_b32 m0, s52
	ds_read_b128 v[34:37], v144 offset:49152
	ds_read_b128 v[38:41], v144 offset:50176
	ds_read_b128 v[162:165], v144 offset:51200
	ds_read_b128 v[166:169], v144 offset:52224
	ds_read_b128 v[170:173], v144 offset:53248
	ds_read_b128 v[174:177], v144 offset:54272
	ds_read_b128 v[178:181], v144 offset:55296
	ds_read_b128 v[182:185], v144 offset:56320
	global_load_lds_dwordx4 v[10:11], off
	v_lshl_add_u64 v[10:11], v[134:135], 0, s[20:21]
	s_add_i32 m0, s52, 0x2000
	s_add_i32 s52, s53, s57
	global_load_lds_dwordx4 v[10:11], off
	v_lshl_add_u64 v[10:11], v[134:135], 0, s[22:23]
	s_mov_b32 m0, s52
	s_nop 0
	global_load_lds_dwordx4 v[10:11], off
	v_lshl_add_u64 v[10:11], v[134:135], 0, s[28:29]
	s_add_i32 m0, s52, 0x2000
	s_nop 0
	global_load_lds_dwordx4 v[10:11], off
	v_lshl_add_u64 v[10:11], v[136:137], 0, s[18:19]
	s_mov_b32 m0, s62
	s_nop 0
	global_load_lds_dwordx4 v[10:11], off
	v_lshl_add_u64 v[10:11], v[136:137], 0, s[20:21]
	s_mov_b32 m0, s63
	s_nop 0
	global_load_lds_dwordx4 v[10:11], off
	s_waitcnt vmcnt(8)
	s_waitcnt lgkmcnt(0)
	s_barrier
	s_setprio 1
	s_waitcnt lgkmcnt(0)
	v_mfma_scale_f32_16x16x128_f8f6f4 v[62:65], v[2:9], v[34:41], v[62:65], v145, v145 op_sel:[0,1,0] op_sel_hi:[0,0,0]
	v_mfma_scale_f32_16x16x128_f8f6f4 v[58:61], v[18:25], v[34:41], v[58:61], v145, v145 op_sel:[0,1,0] op_sel_hi:[0,0,0]
	v_mfma_scale_f32_16x16x128_f8f6f4 v[46:49], v[2:9], v[162:169], v[194:197], v145, v145 op_sel:[0,1,0] op_sel_hi:[0,0,0]
	v_mfma_scale_f32_16x16x128_f8f6f4 v[42:45], v[18:25], v[162:169], v[198:201], v145, v145 op_sel:[0,1,0] op_sel_hi:[0,0,0]
	v_mfma_scale_f32_16x16x128_f8f6f4 v[30:33], v[2:9], v[170:177], v[202:205], v145, v145 op_sel:[0,1,0] op_sel_hi:[0,0,0]
	v_mfma_scale_f32_16x16x128_f8f6f4 v[26:29], v[18:25], v[170:177], v[206:209], v145, v145 op_sel:[0,1,0] op_sel_hi:[0,0,0]
	v_mfma_scale_f32_16x16x128_f8f6f4 v[14:17], v[2:9], v[178:185], v[222:225], v145, v145 op_sel:[0,1,0] op_sel_hi:[0,0,0]
	v_mfma_scale_f32_16x16x128_f8f6f4 v[10:13], v[18:25], v[178:185], v[226:229], v145, v145 op_sel:[0,1,0] op_sel_hi:[0,0,0]
	s_setprio 0
	s_setprio 1
	v_mfma_scale_f32_16x16x128_f8f6f4 v[54:57], v[146:153], v[34:41], v[54:57], v145, v145 op_sel:[0,1,0] op_sel_hi:[0,0,0]
	v_mfma_scale_f32_16x16x128_f8f6f4 v[50:53], v[154:161], v[34:41], v[50:53], v145, v145 op_sel:[0,1,0] op_sel_hi:[0,0,0]
	v_mfma_scale_f32_16x16x128_f8f6f4 v[38:41], v[146:153], v[162:169], v[230:233], v145, v145 op_sel:[0,1,0] op_sel_hi:[0,0,0]
	v_mfma_scale_f32_16x16x128_f8f6f4 v[34:37], v[154:161], v[162:169], v[234:237], v145, v145 op_sel:[0,1,0] op_sel_hi:[0,0,0]
	v_mfma_scale_f32_16x16x128_f8f6f4 v[22:25], v[146:153], v[170:177], v[238:241], v145, v145 op_sel:[0,1,0] op_sel_hi:[0,0,0]
	v_mfma_scale_f32_16x16x128_f8f6f4 v[18:21], v[154:161], v[170:177], v[242:245], v145, v145 op_sel:[0,1,0] op_sel_hi:[0,0,0]
	v_mfma_scale_f32_16x16x128_f8f6f4 v[6:9], v[146:153], v[178:185], v[246:249], v145, v145 op_sel:[0,1,0] op_sel_hi:[0,0,0]
	v_mfma_scale_f32_16x16x128_f8f6f4 v[2:5], v[154:161], v[178:185], v[250:253], v145, v145 op_sel:[0,1,0] op_sel_hi:[0,0,0]
	s_setprio 0
	s_add_i32 s80, s80, 2
	s_add_u32 s50, s50, 0x100
	s_addc_u32 s51, s51, 0
	s_add_u32 s78, s78, 0x100
	s_addc_u32 s79, s79, 0
	s_cmp_gt_u32 s80, 29
	s_barrier
	s_cbranch_scc0 .LBB0_3064
	s_and_b64 vcc, exec, s[30:31]
	s_cbranch_vccz .LBB0_3067
	s_barrier

; #define PG8_STAGE(bufoff, gbase, voff) do { _Pragma("unroll") for (int _i = 0; _i < 2; ++_i) \
;         __builtin_amdgcn_global_load_lds((const unsigned*)((const char*)(gbase) + _i * rstep64 + (voff)), (PG8_LAS unsigned*)(lds + (bufoff) + ldsw + _i * 8192), 16, 0, 0); } while (0)
; #define PG8_WAIT_V(n) asm volatile("s_waitcnt vmcnt(" #n ")" ::: "memory")
; #define PG8_WAIT_L(n) asm volatile("s_waitcnt lgkmcnt(" #n ")" ::: "memory")
; #define PG8_BAR __builtin_amdgcn_s_barrier()
; #define PG8_SCHED __builtin_amdgcn_sched_barrier(0)
;     ...
;             const char* a1 = cA + (size_t)(t + 1) * kstep;
;             const char* a2 = last ? nA : cA + (size_t)(t + 2) * kstep; const char* b2 = last ? nB : cB + (size_t)(t + 2) * kstep;
;             const char* a3 = a2 + kstep; const char* b3 = b2 + kstep;
;             if (last && has_next) S.a_ready(nxt);
;             if constexpr (SP2) {
;             PG8_LDB(B0, 0, 0); PG8_LDB(B1, 0, 1); PG8_SCHED; PG8_LDA(At, 0, 0); PG8_STAGE(PG8_SA(1, 1), a1 + hstep, voffA);
;             PG8_WAIT_V(8); PG8_WAIT_L(0); PG8_BAR; PG8_MMA(0, 0, At, B0); PG8_MMA(0, 1, At, B1); PG8_BAR; PG8_SCHED;
;             PG8_LDA(At, 0, 1); PG8_STAGE(PG8_SB(0, 0), b2, voffB); PG8_STAGE(PG8_SB(0, 1), b2 + hstep, voffB); PG8_STAGE(PG8_SA(0, 0), a2, voffA);
.LBB0_3151:
	ds_read_b128 v[146:149], v142
	ds_read_b128 v[150:153], v142 offset:1024
	ds_read_b128 v[154:157], v142 offset:2048
	ds_read_b128 v[158:161], v142 offset:3072
	ds_read_b128 v[162:165], v143
	ds_read_b128 v[166:169], v143 offset:1024
	ds_read_b128 v[170:173], v143 offset:2048
	ds_read_b128 v[174:177], v143 offset:3072
	s_add_u32 s79, s48, 0xfff00080
	s_addc_u32 s80, s49, -1
	s_cmp_eq_u32 s78, 60
	s_cselect_b32 s81, s41, s80
	s_cselect_b32 s80, s75, s79
	s_cselect_b32 s83, s39, s51
	s_cselect_b32 s82, s77, s50
	v_lshl_add_u64 v[140:141], s[48:49], 0, v[134:135]
	s_add_i32 m0, s47, 0xc000
	ds_read_b128 v[178:181], v144
	ds_read_b128 v[182:185], v144 offset:1024
	ds_read_b128 v[186:189], v144 offset:2048
	ds_read_b128 v[190:193], v144 offset:3072
	ds_read_b128 v[194:197], v144 offset:4096
	ds_read_b128 v[198:201], v144 offset:5120
	ds_read_b128 v[202:205], v144 offset:6144
	ds_read_b128 v[206:209], v144 offset:7168
	global_load_lds_dwordx4 v[140:141], off
	v_lshl_add_u64 v[140:141], v[140:141], 0, s[4:5]
	s_add_i32 m0, s47, 0xe000
	s_nop 0
	global_load_lds_dwordx4 v[140:141], off
	s_waitcnt vmcnt(8)
	s_waitcnt lgkmcnt(0)
	s_barrier
	s_setprio 1
	s_waitcnt lgkmcnt(0)
	v_mfma_f32_16x16x32_bf16 v[126:129], v[146:149], v[178:181], v[126:129]
	v_mfma_f32_16x16x32_bf16 v[122:125], v[154:157], v[178:181], v[122:125]
	v_mfma_f32_16x16x32_bf16 v[118:121], v[146:149], v[186:189], v[118:121]
	v_mfma_f32_16x16x32_bf16 v[110:113], v[154:157], v[186:189], v[110:113]
	v_mfma_f32_16x16x32_bf16 v[102:105], v[146:149], v[194:197], v[102:105]
	v_mfma_f32_16x16x32_bf16 v[94:97], v[154:157], v[194:197], v[94:97]
	v_mfma_f32_16x16x32_bf16 v[86:89], v[146:149], v[202:205], v[86:89]
	v_mfma_f32_16x16x32_bf16 v[78:81], v[154:157], v[202:205], v[78:81]
	v_mfma_f32_16x16x32_bf16 v[126:129], v[150:153], v[182:185], v[126:129]
	v_mfma_f32_16x16x32_bf16 v[122:125], v[158:161], v[182:185], v[122:125]
	v_mfma_f32_16x16x32_bf16 v[118:121], v[150:153], v[190:193], v[118:121]
	v_mfma_f32_16x16x32_bf16 v[110:113], v[158:161], v[190:193], v[110:113]
	v_mfma_f32_16x16x32_bf16 v[102:105], v[150:153], v[198:201], v[102:105]
	v_mfma_f32_16x16x32_bf16 v[94:97], v[158:161], v[198:201], v[94:97]
	v_mfma_f32_16x16x32_bf16 v[86:89], v[150:153], v[206:209], v[86:89]
	v_mfma_f32_16x16x32_bf16 v[78:81], v[158:161], v[206:209], v[78:81]
	s_setprio 0
	s_setprio 1
	v_mfma_f32_16x16x32_bf16 v[114:117], v[162:165], v[178:181], v[114:117]
	v_mfma_f32_16x16x32_bf16 v[106:109], v[170:173], v[178:181], v[106:109]
	v_mfma_f32_16x16x32_bf16 v[98:101], v[162:165], v[186:189], v[98:101]
	v_mfma_f32_16x16x32_bf16 v[90:93], v[170:173], v[186:189], v[90:93]
	v_mfma_f32_16x16x32_bf16 v[82:85], v[162:165], v[194:197], v[82:85]
	v_mfma_f32_16x16x32_bf16 v[74:77], v[170:173], v[194:197], v[74:77]
	v_mfma_f32_16x16x32_bf16 v[70:73], v[162:165], v[202:205], v[70:73]
	v_mfma_f32_16x16x32_bf16 v[66:69], v[170:173], v[202:205], v[66:69]
	v_mfma_f32_16x16x32_bf16 v[114:117], v[166:169], v[182:185], v[114:117]
	v_mfma_f32_16x16x32_bf16 v[106:109], v[174:177], v[182:185], v[106:109]
	v_mfma_f32_16x16x32_bf16 v[98:101], v[166:169], v[190:193], v[98:101]
	v_mfma_f32_16x16x32_bf16 v[90:93], v[174:177], v[190:193], v[90:93]
	v_mfma_f32_16x16x32_bf16 v[82:85], v[166:169], v[198:201], v[82:85]
	v_mfma_f32_16x16x32_bf16 v[74:77], v[174:177], v[198:201], v[74:77]
	v_mfma_f32_16x16x32_bf16 v[70:73], v[166:169], v[206:209], v[70:73]
	v_mfma_f32_16x16x32_bf16 v[66:69], v[174:177], v[206:209], v[66:69]
	s_setprio 0
	s_barrier
	s_add_i32 s79, s64, s53
	v_lshl_add_u64 v[140:141], s[82:83], 0, v[130:131]
	s_mov_b32 m0, s79
	ds_read_b128 v[178:181], v144 offset:16384
	ds_read_b128 v[182:185], v144 offset:17408
	ds_read_b128 v[186:189], v144 offset:18432
	ds_read_b128 v[190:193], v144 offset:19456
	ds_read_b128 v[194:197], v144 offset:20480
	ds_read_b128 v[198:201], v144 offset:21504
	ds_read_b128 v[202:205], v144 offset:22528
	ds_read_b128 v[206:209], v144 offset:23552
	global_load_lds_dwordx4 v[140:141], off
	v_lshl_add_u64 v[210:211], v[140:141], 0, s[4:5]
	s_add_i32 m0, s79, 0x2000
	s_add_i32 s79, s65, s53
	global_load_lds_dwordx4 v[210:211], off
	v_lshl_add_u64 v[210:211], v[140:141], 0, s[6:7]
	s_mov_b32 m0, s79
	s_nop 0
	global_load_lds_dwordx4 v[210:211], off
	v_lshl_add_u64 v[210:211], v[140:141], 0, s[8:9]
	s_add_i32 m0, s79, 0x2000
	s_nop 0
	global_load_lds_dwordx4 v[210:211], off
	v_lshl_add_u64 v[210:211], s[80:81], 0, v[132:133]
	s_mov_b32 m0, s47
	v_lshl_add_u64 v[212:213], v[210:211], 0, s[4:5]
	global_load_lds_dwordx4 v[210:211], off
	s_mov_b32 m0, s55
	s_nop 0
	global_load_lds_dwordx4 v[212:213], off
	s_waitcnt vmcnt(8)
	s_waitcnt lgkmcnt(0)
	s_barrier
; #define PG8_STAGE(bufoff, gbase, voff) do { _Pragma("unroll") for (int _i = 0; _i < 2; ++_i) \
;         __builtin_amdgcn_global_load_lds((const unsigned*)((const char*)(gbase) + _i * rstep64 + (voff)), (PG8_LAS unsigned*)(lds + (bufoff) + ldsw + _i * 8192), 16, 0, 0); } while (0)
; #define PG8_WAIT_V(n) asm volatile("s_waitcnt vmcnt(" #n ")" ::: "memory")
; #define PG8_WAIT_L(n) asm volatile("s_waitcnt lgkmcnt(" #n ")" ::: "memory")
; #define PG8_BAR __builtin_amdgcn_s_barrier()
; #define PG8_SCHED __builtin_amdgcn_sched_barrier(0)
;     ...
;             PG8_LDB(B0, 0, 0); PG8_LDB(B1, 0, 1); PG8_SCHED; PG8_LDA(At, 0, 0); PG8_STAGE(PG8_SA(1, 1), a1 + hstep, voffA);
;             PG8_WAIT_V(8); PG8_WAIT_L(0); PG8_BAR; PG8_MMA(0, 0, At, B0); PG8_MMA(0, 1, At, B1); PG8_BAR; PG8_SCHED;
;             PG8_LDA(At, 0, 1); PG8_STAGE(PG8_SB(0, 0), b2, voffB); PG8_STAGE(PG8_SB(0, 1), b2 + hstep, voffB); PG8_STAGE(PG8_SA(0, 0), a2, voffA);
;             PG8_WAIT_V(8); PG8_WAIT_L(0); PG8_BAR; PG8_MMA(1, 0, At, B0); PG8_MMA(1, 1, At, B1); PG8_BAR; PG8_SCHED;
;             PG8_LDB(B0, 1, 0); PG8_LDB(B1, 1, 1); PG8_SCHED; PG8_LDA(At, 1, 0); PG8_STAGE(PG8_SA(0, 1), a2 + hstep, voffA);
;             PG8_WAIT_V(8); PG8_WAIT_L(0); PG8_BAR; PG8_MMA(0, 0, At, B0); PG8_MMA(0, 1, At, B1); PG8_BAR; PG8_SCHED;
;             PG8_LDA(At, 1, 1); PG8_STAGE(PG8_SB(1, 0), b3, voffB); PG8_STAGE(PG8_SB(1, 1), b3 + hstep, voffB); PG8_STAGE(PG8_SA(1, 0), a3, voffA);
;             PG8_WAIT_V(8); PG8_WAIT_L(0); PG8_BAR; PG8_MMA(1, 0, At, B0); PG8_MMA(1, 1, At, B1); PG8_BAR; PG8_SCHED;
	s_setprio 1
	s_waitcnt lgkmcnt(0)
	v_mfma_f32_16x16x32_bf16 v[62:65], v[146:149], v[178:181], v[62:65]
	v_mfma_f32_16x16x32_bf16 v[58:61], v[154:157], v[178:181], v[58:61]
	v_mfma_f32_16x16x32_bf16 v[54:57], v[146:149], v[186:189], v[54:57]
	v_mfma_f32_16x16x32_bf16 v[46:49], v[154:157], v[186:189], v[46:49]
	v_mfma_f32_16x16x32_bf16 v[38:41], v[146:149], v[194:197], v[38:41]
	v_mfma_f32_16x16x32_bf16 v[30:33], v[154:157], v[194:197], v[30:33]
	v_mfma_f32_16x16x32_bf16 v[22:25], v[146:149], v[202:205], v[22:25]
	v_mfma_f32_16x16x32_bf16 v[14:17], v[154:157], v[202:205], v[14:17]
	v_mfma_f32_16x16x32_bf16 v[62:65], v[150:153], v[182:185], v[62:65]
	v_mfma_f32_16x16x32_bf16 v[58:61], v[158:161], v[182:185], v[58:61]
	v_mfma_f32_16x16x32_bf16 v[54:57], v[150:153], v[190:193], v[54:57]
	v_mfma_f32_16x16x32_bf16 v[46:49], v[158:161], v[190:193], v[46:49]
	v_mfma_f32_16x16x32_bf16 v[38:41], v[150:153], v[198:201], v[38:41]
	v_mfma_f32_16x16x32_bf16 v[30:33], v[158:161], v[198:201], v[30:33]
	v_mfma_f32_16x16x32_bf16 v[22:25], v[150:153], v[206:209], v[22:25]
	v_mfma_f32_16x16x32_bf16 v[14:17], v[158:161], v[206:209], v[14:17]
	s_setprio 0
	s_setprio 1
	v_mfma_f32_16x16x32_bf16 v[50:53], v[162:165], v[178:181], v[50:53]
	v_mfma_f32_16x16x32_bf16 v[42:45], v[170:173], v[178:181], v[42:45]
	v_mfma_f32_16x16x32_bf16 v[34:37], v[162:165], v[186:189], v[34:37]
	v_mfma_f32_16x16x32_bf16 v[26:29], v[170:173], v[186:189], v[26:29]
	v_mfma_f32_16x16x32_bf16 v[18:21], v[162:165], v[194:197], v[18:21]
	v_mfma_f32_16x16x32_bf16 v[10:13], v[170:173], v[194:197], v[10:13]
	v_mfma_f32_16x16x32_bf16 v[6:9], v[162:165], v[202:205], v[6:9]
	v_mfma_f32_16x16x32_bf16 v[2:5], v[170:173], v[202:205], v[2:5]
	v_mfma_f32_16x16x32_bf16 v[50:53], v[166:169], v[182:185], v[50:53]
	v_mfma_f32_16x16x32_bf16 v[42:45], v[174:177], v[182:185], v[42:45]
	v_mfma_f32_16x16x32_bf16 v[34:37], v[166:169], v[190:193], v[34:37]
	v_mfma_f32_16x16x32_bf16 v[26:29], v[174:177], v[190:193], v[26:29]
	v_mfma_f32_16x16x32_bf16 v[18:21], v[166:169], v[198:201], v[18:21]
	v_mfma_f32_16x16x32_bf16 v[10:13], v[174:177], v[198:201], v[10:13]
	v_mfma_f32_16x16x32_bf16 v[6:9], v[166:169], v[206:209], v[6:9]
	v_mfma_f32_16x16x32_bf16 v[2:5], v[174:177], v[206:209], v[2:5]
	s_setprio 0
	s_barrier
	s_add_i32 s79, 0, 0x18000
	v_add_u32_e32 v145, s79, v1
	s_add_i32 s80, 0, 0x1c000
	ds_read_b128 v[146:149], v145
	ds_read_b128 v[150:153], v145 offset:1024
	ds_read_b128 v[154:157], v145 offset:2048
	ds_read_b128 v[158:161], v145 offset:3072
	v_add_u32_e32 v145, s80, v1
	ds_read_b128 v[162:165], v145
	ds_read_b128 v[166:169], v145 offset:1024
	ds_read_b128 v[170:173], v145 offset:2048
	ds_read_b128 v[174:177], v145 offset:3072
	s_mov_b32 m0, s56
	v_lshl_add_u64 v[212:213], v[210:211], 0, s[6:7]
	ds_read_b128 v[178:181], v144 offset:32768
	ds_read_b128 v[182:185], v144 offset:33792
	ds_read_b128 v[186:189], v144 offset:34816
	ds_read_b128 v[190:193], v144 offset:35840
	ds_read_b128 v[194:197], v144 offset:36864
	ds_read_b128 v[198:201], v144 offset:37888
	ds_read_b128 v[202:205], v144 offset:38912
	ds_read_b128 v[206:209], v144 offset:39936
	global_load_lds_dwordx4 v[212:213], off
	v_lshl_add_u64 v[212:213], v[210:211], 0, s[8:9]
	s_mov_b32 m0, s57
	s_nop 0
	global_load_lds_dwordx4 v[212:213], off
	s_waitcnt vmcnt(8)
	s_waitcnt lgkmcnt(0)
	s_barrier
	s_setprio 1
	s_waitcnt lgkmcnt(0)
	v_mfma_f32_16x16x32_bf16 v[126:129], v[146:149], v[178:181], v[126:129]
	v_mfma_f32_16x16x32_bf16 v[122:125], v[154:157], v[178:181], v[122:125]
	v_mfma_f32_16x16x32_bf16 v[118:121], v[146:149], v[186:189], v[118:121]
	v_mfma_f32_16x16x32_bf16 v[110:113], v[154:157], v[186:189], v[110:113]
	v_mfma_f32_16x16x32_bf16 v[102:105], v[146:149], v[194:197], v[102:105]
	v_mfma_f32_16x16x32_bf16 v[94:97], v[154:157], v[194:197], v[94:97]
	v_mfma_f32_16x16x32_bf16 v[86:89], v[146:149], v[202:205], v[86:89]
	v_mfma_f32_16x16x32_bf16 v[78:81], v[154:157], v[202:205], v[78:81]
	v_mfma_f32_16x16x32_bf16 v[126:129], v[150:153], v[182:185], v[126:129]
	v_mfma_f32_16x16x32_bf16 v[122:125], v[158:161], v[182:185], v[122:125]
	v_mfma_f32_16x16x32_bf16 v[118:121], v[150:153], v[190:193], v[118:121]
	v_mfma_f32_16x16x32_bf16 v[110:113], v[158:161], v[190:193], v[110:113]
	v_mfma_f32_16x16x32_bf16 v[102:105], v[150:153], v[198:201], v[102:105]
	v_mfma_f32_16x16x32_bf16 v[94:97], v[158:161], v[198:201], v[94:97]
	v_mfma_f32_16x16x32_bf16 v[86:89], v[150:153], v[206:209], v[86:89]
	v_mfma_f32_16x16x32_bf16 v[78:81], v[158:161], v[206:209], v[78:81]
	s_setprio 0
	s_setprio 1
	v_mfma_f32_16x16x32_bf16 v[114:117], v[162:165], v[178:181], v[114:117]
	v_mfma_f32_16x16x32_bf16 v[106:109], v[170:173], v[178:181], v[106:109]
	v_mfma_f32_16x16x32_bf16 v[98:101], v[162:165], v[186:189], v[98:101]
	v_mfma_f32_16x16x32_bf16 v[90:93], v[170:173], v[186:189], v[90:93]
	v_mfma_f32_16x16x32_bf16 v[82:85], v[162:165], v[194:197], v[82:85]
	v_mfma_f32_16x16x32_bf16 v[74:77], v[170:173], v[194:197], v[74:77]
	v_mfma_f32_16x16x32_bf16 v[70:73], v[162:165], v[202:205], v[70:73]
	v_mfma_f32_16x16x32_bf16 v[66:69], v[170:173], v[202:205], v[66:69]
	v_mfma_f32_16x16x32_bf16 v[114:117], v[166:169], v[182:185], v[114:117]
	v_mfma_f32_16x16x32_bf16 v[106:109], v[174:177], v[182:185], v[106:109]
	v_mfma_f32_16x16x32_bf16 v[98:101], v[166:169], v[190:193], v[98:101]
	v_mfma_f32_16x16x32_bf16 v[90:93], v[174:177], v[190:193], v[90:93]
	v_mfma_f32_16x16x32_bf16 v[82:85], v[166:169], v[198:201], v[82:85]
	v_mfma_f32_16x16x32_bf16 v[74:77], v[174:177], v[198:201], v[74:77]
	v_mfma_f32_16x16x32_bf16 v[70:73], v[166:169], v[206:209], v[70:73]
	v_mfma_f32_16x16x32_bf16 v[66:69], v[174:177], v[206:209], v[66:69]
	s_setprio 0
	s_barrier
; #define PG8_STAGE(bufoff, gbase, voff) do { _Pragma("unroll") for (int _i = 0; _i < 2; ++_i) \
;         __builtin_amdgcn_global_load_lds((const unsigned*)((const char*)(gbase) + _i * rstep64 + (voff)), (PG8_LAS unsigned*)(lds + (bufoff) + ldsw + _i * 8192), 16, 0, 0); } while (0)
; #define PG8_WAIT_V(n) asm volatile("s_waitcnt vmcnt(" #n ")" ::: "memory")
; #define PG8_WAIT_L(n) asm volatile("s_waitcnt lgkmcnt(" #n ")" ::: "memory")
; #define PG8_BAR __builtin_amdgcn_s_barrier()
; #define PG8_SCHED __builtin_amdgcn_sched_barrier(0)
;     ...
;             PG8_WAIT_V(8); PG8_WAIT_L(0); PG8_BAR; PG8_MMA(1, 0, At, B0); PG8_MMA(1, 1, At, B1); PG8_BAR; PG8_SCHED;
;             PG8_LDB(B0, 1, 0); PG8_LDB(B1, 1, 1); PG8_SCHED; PG8_LDA(At, 1, 0); PG8_STAGE(PG8_SA(0, 1), a2 + hstep, voffA);
;             PG8_WAIT_V(8); PG8_WAIT_L(0); PG8_BAR; PG8_MMA(0, 0, At, B0); PG8_MMA(0, 1, At, B1); PG8_BAR; PG8_SCHED;
;             PG8_LDA(At, 1, 1); PG8_STAGE(PG8_SB(1, 0), b3, voffB); PG8_STAGE(PG8_SB(1, 1), b3 + hstep, voffB); PG8_STAGE(PG8_SA(1, 0), a3, voffA);
;             PG8_WAIT_V(8); PG8_WAIT_L(0); PG8_BAR; PG8_MMA(1, 0, At, B0); PG8_MMA(1, 1, At, B1); PG8_BAR; PG8_SCHED;
	s_add_i32 s79, s79, s53
	v_lshl_add_u64 v[212:213], v[140:141], 0, s[14:15]
	s_mov_b32 m0, s79
	ds_read_b128 v[178:181], v144 offset:49152
	ds_read_b128 v[182:185], v144 offset:50176
	ds_read_b128 v[186:189], v144 offset:51200
	ds_read_b128 v[190:193], v144 offset:52224
	ds_read_b128 v[194:197], v144 offset:53248
	ds_read_b128 v[198:201], v144 offset:54272
	ds_read_b128 v[202:205], v144 offset:55296
	ds_read_b128 v[206:209], v144 offset:56320
	global_load_lds_dwordx4 v[212:213], off
	v_lshl_add_u64 v[212:213], v[140:141], 0, s[16:17]
	s_add_i32 m0, s79, 0x2000
	s_add_i32 s79, s80, s53
	global_load_lds_dwordx4 v[212:213], off
	v_lshl_add_u64 v[212:213], v[140:141], 0, s[18:19]
	s_mov_b32 m0, s79
	v_lshl_add_u64 v[140:141], v[140:141], 0, s[20:21]
	global_load_lds_dwordx4 v[212:213], off
	s_add_i32 m0, s79, 0x2000
	s_nop 0
	global_load_lds_dwordx4 v[140:141], off
	v_lshl_add_u64 v[140:141], v[210:211], 0, s[14:15]
	s_mov_b32 m0, s59
	s_nop 0
	global_load_lds_dwordx4 v[140:141], off
	v_lshl_add_u64 v[140:141], v[210:211], 0, s[16:17]
	s_mov_b32 m0, s60
	s_nop 0
	global_load_lds_dwordx4 v[140:141], off
	s_waitcnt vmcnt(8)
	s_waitcnt lgkmcnt(0)
	s_barrier
	s_setprio 1
	s_waitcnt lgkmcnt(0)
	v_mfma_f32_16x16x32_bf16 v[62:65], v[146:149], v[178:181], v[62:65]
	v_mfma_f32_16x16x32_bf16 v[58:61], v[154:157], v[178:181], v[58:61]
	v_mfma_f32_16x16x32_bf16 v[54:57], v[146:149], v[186:189], v[54:57]
	v_mfma_f32_16x16x32_bf16 v[46:49], v[154:157], v[186:189], v[46:49]
	v_mfma_f32_16x16x32_bf16 v[38:41], v[146:149], v[194:197], v[38:41]
	v_mfma_f32_16x16x32_bf16 v[30:33], v[154:157], v[194:197], v[30:33]
	v_mfma_f32_16x16x32_bf16 v[22:25], v[146:149], v[202:205], v[22:25]
	v_mfma_f32_16x16x32_bf16 v[14:17], v[154:157], v[202:205], v[14:17]
	v_mfma_f32_16x16x32_bf16 v[62:65], v[150:153], v[182:185], v[62:65]
	v_mfma_f32_16x16x32_bf16 v[58:61], v[158:161], v[182:185], v[58:61]
	v_mfma_f32_16x16x32_bf16 v[54:57], v[150:153], v[190:193], v[54:57]
	v_mfma_f32_16x16x32_bf16 v[46:49], v[158:161], v[190:193], v[46:49]
	v_mfma_f32_16x16x32_bf16 v[38:41], v[150:153], v[198:201], v[38:41]
	v_mfma_f32_16x16x32_bf16 v[30:33], v[158:161], v[198:201], v[30:33]
	v_mfma_f32_16x16x32_bf16 v[22:25], v[150:153], v[206:209], v[22:25]
	v_mfma_f32_16x16x32_bf16 v[14:17], v[158:161], v[206:209], v[14:17]
	s_setprio 0
	s_setprio 1
	v_mfma_f32_16x16x32_bf16 v[50:53], v[162:165], v[178:181], v[50:53]
	v_mfma_f32_16x16x32_bf16 v[42:45], v[170:173], v[178:181], v[42:45]
	v_mfma_f32_16x16x32_bf16 v[34:37], v[162:165], v[186:189], v[34:37]
	v_mfma_f32_16x16x32_bf16 v[26:29], v[170:173], v[186:189], v[26:29]
	v_mfma_f32_16x16x32_bf16 v[18:21], v[162:165], v[194:197], v[18:21]
	v_mfma_f32_16x16x32_bf16 v[10:13], v[170:173], v[194:197], v[10:13]
	v_mfma_f32_16x16x32_bf16 v[6:9], v[162:165], v[202:205], v[6:9]
	v_mfma_f32_16x16x32_bf16 v[2:5], v[170:173], v[202:205], v[2:5]
	v_mfma_f32_16x16x32_bf16 v[50:53], v[166:169], v[182:185], v[50:53]
	v_mfma_f32_16x16x32_bf16 v[42:45], v[174:177], v[182:185], v[42:45]
	v_mfma_f32_16x16x32_bf16 v[34:37], v[166:169], v[190:193], v[34:37]
	v_mfma_f32_16x16x32_bf16 v[26:29], v[174:177], v[190:193], v[26:29]
	v_mfma_f32_16x16x32_bf16 v[18:21], v[166:169], v[198:201], v[18:21]
	v_mfma_f32_16x16x32_bf16 v[10:13], v[174:177], v[198:201], v[10:13]
	v_mfma_f32_16x16x32_bf16 v[6:9], v[166:169], v[206:209], v[6:9]
	v_mfma_f32_16x16x32_bf16 v[2:5], v[174:177], v[206:209], v[2:5]
	s_setprio 0
	s_add_i32 s78, s78, 2
	s_add_u32 s48, s48, 0x100
	s_addc_u32 s49, s49, 0
	s_add_u32 s50, s50, 0x100
	s_addc_u32 s51, s51, 0
	s_cmp_gt_u32 s78, 61
	s_barrier
	s_cbranch_scc0 .LBB0_3151
	s_and_b64 vcc, exec, s[22:23]
	s_cbranch_vccz .LBB0_3154
	s_barrier
